# GU unit top: counted vmcnt(8) for the gather index loads instead of vmcnt(0) (does not drain the previous epilogue stores)
# speedup vs baseline: 1.0163x; 1.0163x over previous
.LBB0_744:
	v_cndmask_b32_e64 v2, 0, 1, s[38:39]
	v_cmp_ne_u32_e64 s[6:7], 1, v2
	v_add_u32_e32 v2, 0, v234
	s_andn2_b64 vcc, exec, s[38:39]
	v_add_u32_e32 v253, 0x24400, v2
	s_cbranch_vccnz .LBB0_746
	s_cmp_eq_u64 s[34:35], 0
	v_add_u32_e32 v2, v251, v235
	s_cselect_b64 vcc, -1, 0
	s_cmp_lg_u32 s65, 1
	s_cbranch_scc1 .Lgu_w8
	s_waitcnt vmcnt(0)
	s_branch .Lgu_wd
.Lgu_w8:
	s_waitcnt vmcnt(8)
.Lgu_wd:
	v_cndmask_b32_e32 v3, v241, v2, vcc
	v_cmp_lt_i32_e64 s[8:9], v2, v252
	s_nop 1
	v_cndmask_b32_e64 v2, 0, v3, s[8:9]
	v_add_u32_e32 v3, v251, v237
	v_cndmask_b32_e32 v4, v243, v3, vcc
	v_cmp_lt_i32_e64 s[8:9], v3, v252
	v_mul_lo_u32 v2, v2, s14
	v_add_lshl_u32 v2, v2, v236, 1
	v_cndmask_b32_e64 v3, 0, v4, s[8:9]
	v_add_u32_e32 v4, v251, v239
	v_cndmask_b32_e32 v5, v245, v4, vcc
	v_cmp_lt_i32_e64 s[8:9], v4, v252
	v_mul_lo_u32 v3, v3, s14
	v_add_lshl_u32 v3, v3, v238, 1
	v_cndmask_b32_e64 v4, 0, v5, s[8:9]
	v_add_u32_e32 v5, v251, v240
	v_cndmask_b32_e32 v6, v248, v5, vcc
	v_cmp_lt_i32_e32 vcc, v5, v252
	v_mul_lo_u32 v4, v4, s14
	v_add_lshl_u32 v4, v4, v236, 1
	v_cndmask_b32_e32 v5, 0, v6, vcc
	v_mul_lo_u32 v5, v5, s14
	v_add_lshl_u32 v5, v5, v238, 1
	ds_write_b128 v253, v[2:5]
